# phases 9 and 10 reuse the MoE tile table left in LDS by phase 8 (rebuild skipped)
# speedup vs baseline: 1.0117x; 1.0117x over previous
.LBB0_1534:
	s_andn2_b64 vcc, exec, s[2:3]
	s_cbranch_vccnz .LBB0_1640
	v_readlane_b32 s10, v252, 0
	v_readlane_b32 s11, v252, 1
	s_waitcnt vmcnt(0) expcnt(0) lgkmcnt(0)
	s_load_dwordx2 s[8:9], s[10:11], 0x98
	v_mbcnt_lo_u32_b32 v0, -1, 0
	v_mbcnt_hi_u32_b32 v0, -1, v0
	s_nop 0
	v_add_u32_e32 v130, s93, v0
	s_nop 0
	v_readfirstlane_b32 s52, v130
	s_branch .Lskip_tab9
	v_cmp_gt_i32_e32 vcc, 64, v130
	s_and_saveexec_b64 s[12:13], vcc
	s_cbranch_execz .LBB0_1542
	v_cmp_gt_i32_e64 s[2:3], 32, v130
	v_mov_b32_e32 v1, 0
	s_and_saveexec_b64 s[4:5], s[2:3]
	s_cbranch_execz .LBB0_1538
	s_lshl_b32 s86, s44, 6
	s_lshl_b64 s[6:7], s[86:87], 2
	s_waitcnt lgkmcnt(0)
	s_add_u32 s6, s8, s6
	s_addc_u32 s7, s9, s7
	v_ashrrev_i32_e32 v131, 31, v130
	v_lshl_add_u64 v[0:1], v[130:131], 2, s[6:7]
	v_add_co_u32_e32 v0, vcc, 0x10000, v0
	s_nop 1
	v_addc_co_u32_e32 v1, vcc, 0, v1, vcc
	global_load_dword v1, v[0:1], off sc1

.Lskip_tab9:
	v_readlane_b32 s2, v253, 62
	s_waitcnt lgkmcnt(0)
	s_barrier
	v_mov_b32_e32 v0, s2
	ds_read_b32 v0, v0
	s_add_u32 s53, s8, 0x23b00000
	s_addc_u32 s54, s9, 0
	s_movk_i32 s12, 0x400
	v_mov_b32_e32 v1, v130
	s_waitcnt lgkmcnt(0)
	v_readfirstlane_b32 s2, v0
	s_lshl_b32 s55, s2, 2
	s_cmp_ge_i32 s90, s55
	v_readfirstlane_b32 s6, v1
	s_cbranch_scc1 .LBB0_1582
	v_bfe_i32 v3, v1, 27, 1
	v_lshlrev_b32_e32 v2, 4, v1
	v_lshrrev_b32_e32 v3, 22, v3
	v_add_u32_e32 v3, v2, v3
	v_and_b32_e32 v3, 0xfffffc00, v3
	v_sub_u32_e32 v3, v2, v3
	v_ashrrev_i32_e32 v0, 31, v1
	v_lshrrev_b32_e32 v4, 4, v3
	v_lshrrev_b32_e32 v0, 26, v0
	v_bitop3_b32 v3, v4, v3, 32 bitop3:0x6c
	v_add_u32_e32 v0, v1, v0
	v_ashrrev_i32_e32 v5, 31, v3
	v_ashrrev_i32_e32 v0, 6, v0
	v_lshrrev_b32_e32 v5, 26, v5
	v_lshlrev_b32_e32 v4, 3, v0
	v_add_u32_e32 v5, v3, v5
	v_and_b32_e32 v4, -16, v4
	v_ashrrev_i32_e32 v6, 6, v5
	v_and_b32_e32 v5, 0xc0, v5
	v_add_u32_e32 v4, v6, v4
	v_sub_u32_e32 v3, v3, v5
	v_lshlrev_b32_e32 v0, 5, v0
	v_ashrrev_i16_sdwa v3, v239, sext(v3) dst_sel:DWORD dst_unused:UNUSED_PAD src0_sel:DWORD src1_sel:BYTE_0
	v_lshlrev_b32_e32 v5, 1, v4
	v_lshlrev_b32_e32 v7, 2, v4
	v_lshrrev_b32_e32 v8, 2, v4
	v_and_b32_e32 v6, 3, v6
	v_and_b32_e32 v0, 32, v0
	v_bfe_i32 v3, v3, 0, 16
	v_and_b32_e32 v5, 0xffffffc0, v5
	v_and_b32_e32 v8, 4, v8
	v_and_or_b32 v6, v7, 48, v6
	v_or3_b32 v5, v6, v5, v8
	v_add_lshl_u32 v0, v0, v3, 1
	v_mad_u64_u32 v[132:133], s[4:5], v4, s12, v[0:1]
	v_mbcnt_lo_u32_b32 v68, -1, 0
	v_mbcnt_hi_u32_b32 v68, -1, v68
	v_add_u32_e32 v68, s93, v68
	v_lshrrev_b32_e32 v69, 3, v68
	v_lshrrev_b32_e32 v70, 4, v68
	v_xor_b32_e32 v70, v70, v68
	v_lshlrev_b32_e32 v70, 4, v70
	v_and_b32_e32 v70, 0x70, v70
	v_lshl_add_u32 v132, v69, 10, v70
	v_mad_u64_u32 v[134:135], s[4:5], v5, s12, v[0:1]
	v_mbcnt_lo_u32_b32 v68, -1, 0
	v_mbcnt_hi_u32_b32 v68, -1, v68
	v_add_u32_e32 v68, s93, v68
	v_lshrrev_b32_e32 v69, 3, v68
	v_and_b32_e32 v70, 0x60, v69
	v_lshlrev_b32_e32 v70, 1, v70
	v_and_or_b32 v70, v69, 3, v70
	v_and_b32_e32 v134, 12, v69
	v_lshl_or_b32 v70, v134, 2, v70
	v_lshrrev_b32_e32 v69, 2, v69
	v_and_b32_e32 v69, 4, v69
	v_or_b32_e32 v69, v69, v70
	v_lshrrev_b32_e32 v70, 4, v68
	v_xor_b32_e32 v70, v70, v68
	v_lshlrev_b32_e32 v70, 4, v70
	v_and_b32_e32 v70, 0x70, v70
	v_lshl_add_u32 v134, v69, 10, v70
	v_add_u32_e32 v0, 0x2000, v2
	v_ashrrev_i32_e32 v2, 31, v0
	v_lshrrev_b32_e32 v2, 22, v2
	v_add_u32_e32 v2, v0, v2
	v_ashrrev_i32_e32 v2, 10, v2
	v_mul_i32_i24_e32 v3, 0x400, v2
	v_sub_u32_e32 v0, v0, v3
	v_lshrrev_b32_e32 v3, 4, v0
	v_bitop3_b32 v0, v3, v0, 32 bitop3:0x6c
	v_ashrrev_i32_e32 v4, 31, v0
	v_lshrrev_b32_e32 v4, 26, v4
	v_lshlrev_b32_e32 v3, 3, v2
	v_add_u32_e32 v4, v0, v4
	v_and_b32_e32 v3, -16, v3
	v_ashrrev_i32_e32 v5, 6, v4
	v_and_b32_e32 v4, 0xc0, v4
	v_add_u32_e32 v3, v5, v3
	v_sub_u32_e32 v0, v0, v4
	v_lshlrev_b32_e32 v2, 5, v2
	v_ashrrev_i16_sdwa v0, v239, sext(v0) dst_sel:DWORD dst_unused:UNUSED_PAD src0_sel:DWORD src1_sel:BYTE_0
	v_lshlrev_b32_e32 v4, 1, v3
	v_lshlrev_b32_e32 v6, 2, v3
	v_lshrrev_b32_e32 v7, 2, v3
	v_and_b32_e32 v5, 3, v5
	v_and_b32_e32 v2, 32, v2
	v_bfe_i32 v0, v0, 0, 16
	v_and_b32_e32 v4, 0xffffffc0, v4
	v_and_b32_e32 v7, 4, v7
	v_and_or_b32 v5, v6, 48, v5
	v_or3_b32 v4, v5, v4, v7
	v_add_lshl_u32 v0, v2, v0, 1
	v_mad_u64_u32 v[136:137], s[4:5], v3, s12, v[0:1]
	v_mbcnt_lo_u32_b32 v68, -1, 0
	v_mbcnt_hi_u32_b32 v68, -1, v68
	v_add_u32_e32 v68, s93, v68
	v_lshrrev_b32_e32 v69, 3, v68
	v_add_u32_e32 v69, 64, v69
	v_lshrrev_b32_e32 v70, 4, v68
	v_xor_b32_e32 v70, v70, v68
	v_lshlrev_b32_e32 v70, 4, v70
	v_and_b32_e32 v70, 0x70, v70
	v_lshl_add_u32 v136, v69, 10, v70
	v_mad_u64_u32 v[138:139], s[4:5], v4, s12, v[0:1]
	v_mbcnt_lo_u32_b32 v68, -1, 0
	v_mbcnt_hi_u32_b32 v68, -1, v68
	v_add_u32_e32 v68, s93, v68
	v_lshrrev_b32_e32 v69, 3, v68
	v_add_u32_e32 v69, 64, v69
	v_and_b32_e32 v70, 0x60, v69
	v_lshlrev_b32_e32 v70, 1, v70
	v_and_or_b32 v70, v69, 3, v70
	v_and_b32_e32 v138, 12, v69
	v_lshl_or_b32 v70, v138, 2, v70
	v_lshrrev_b32_e32 v69, 2, v69
	v_and_b32_e32 v69, 4, v69
	v_or_b32_e32 v69, v69, v70
	v_lshrrev_b32_e32 v70, 4, v68
	v_xor_b32_e32 v70, v70, v68
	v_lshlrev_b32_e32 v70, 4, v70
	v_and_b32_e32 v70, 0x70, v70
	v_lshl_add_u32 v138, v69, 10, v70
	v_readlane_b32 s4, v253, 4
	s_lshl_b32 s86, s44, 15
	s_lshl_b64 s[2:3], s[86:87], 10
	v_mov_b32_e32 v0, s4
	ds_read_b32 v152, v0 offset:1792
	s_add_u32 s56, s53, s2
	s_addc_u32 s57, s54, s3
	v_readlane_b32 s19, v254, 16
	s_add_u32 s58, s8, 0x4e500000
	s_waitcnt lgkmcnt(0)
	v_lshlrev_b32_e32 v0, 2, v152
	v_add_u32_e32 v0, 0, v0
	v_add_u32_e32 v0, 0x20600, v0
	ds_read_b32 v0, v0
	v_mov_b32_e32 v2, s19
	v_readfirstlane_b32 s19, v152
	s_addc_u32 s59, s9, 0
	s_ashr_i32 s13, s12, 31
	ds_read_b32 v2, v2
	s_waitcnt lgkmcnt(1)
	v_readfirstlane_b32 s4, v0
	s_lshl_b32 s19, s19, 8
	s_ashr_i32 s7, s6, 6
	s_ashr_i32 s5, s4, 31
	s_mul_i32 s20, s19, s13
	s_mul_hi_u32 s21, s19, s12
	s_ashr_i32 s24, s6, 8
	s_lshl_b64 s[14:15], s[12:13], 3
	s_lshl_b64 s[16:17], s[12:13], 7
	s_lshl_b32 s18, s7, 10
	s_add_i32 s21, s21, s20
	s_lshl_b64 s[4:5], s[4:5], 20
	s_add_u32 s4, s56, s4
	s_addc_u32 s5, s57, s5
	v_readlane_b32 s22, v253, 7
	v_readlane_b32 s23, v253, 8
	s_add_u32 s40, s4, s22
	s_addc_u32 s41, s5, s23
	s_add_i32 s60, s18, 0
	s_load_dwordx2 s[2:3], s[10:11], 0x78
	s_add_i32 s61, s60, 0x10000
	s_mov_b32 m0, s61
	s_nop 0
	global_load_lds_dwordx4 v134, s[40:41]
	s_add_i32 s62, s60, 0x12000
	s_mov_b32 m0, s62
	s_nop 0
	global_load_lds_dwordx4 v138, s[40:41]
	s_add_u32 s4, s40, s14
	s_mul_i32 s19, s19, s12
	s_addc_u32 s5, s41, s15
	s_add_i32 s63, s60, 0x14000
	s_mov_b32 m0, s63
	s_nop 0
	global_load_lds_dwordx4 v134, s[4:5]
	s_add_i32 s64, s60, 0x16000
	s_mov_b32 m0, s64
	s_nop 0
	global_load_lds_dwordx4 v138, s[4:5]
	s_add_u32 s42, s58, s19
	s_addc_u32 s43, s59, s21
	s_mov_b32 m0, s60
	s_nop 0
	global_load_lds_dwordx4 v132, s[42:43]
	s_add_i32 s65, s60, 0x2000
	s_mov_b32 m0, s65
	s_nop 0
	global_load_lds_dwordx4 v136, s[42:43]
	s_add_u32 s18, s42, s16
	s_addc_u32 s19, s43, s17
	s_add_i32 s66, s60, 0x4000
	s_mov_b32 m0, s66
	s_nop 0
	global_load_lds_dwordx4 v132, s[18:19]
	s_add_i32 s67, s60, 0x6000
	s_mov_b32 m0, s67
	s_nop 0
	global_load_lds_dwordx4 v136, s[18:19]
	s_cmp_eq_u32 s24, 1
	s_cselect_b64 s[18:19], -1, 0
	s_cmp_lg_u32 s24, 1
	s_cbranch_scc1 .LBB0_1554
	s_barrier

.LBB0_1641:
	v_readlane_b32 s12, v252, 0
	v_readlane_b32 s13, v252, 1
	s_waitcnt vmcnt(0) expcnt(0) lgkmcnt(0)
	s_load_dwordx2 s[8:9], s[12:13], 0x98
	v_mbcnt_lo_u32_b32 v0, -1, 0
	v_mbcnt_hi_u32_b32 v0, -1, v0
	s_nop 0
	v_add_u32_e32 v4, s93, v0
	s_nop 0
	v_readfirstlane_b32 s18, v4
	s_branch .Lskip_tab10
	v_cmp_gt_i32_e32 vcc, 64, v4
	s_and_saveexec_b64 s[10:11], vcc
	s_cbranch_execz .LBB0_1648
	v_cmp_gt_i32_e64 s[2:3], 32, v4
	v_mov_b32_e32 v1, 0
	s_and_saveexec_b64 s[4:5], s[2:3]
	s_cbranch_execz .LBB0_1644
	s_lshl_b32 s86, s44, 6
	s_lshl_b64 s[6:7], s[86:87], 2
	s_waitcnt lgkmcnt(0)
	s_add_u32 s6, s8, s6
	s_addc_u32 s7, s9, s7
	v_ashrrev_i32_e32 v5, 31, v4
	v_lshl_add_u64 v[0:1], v[4:5], 2, s[6:7]
	v_add_co_u32_e32 v0, vcc, 0x10000, v0
	s_nop 1
	v_addc_co_u32_e32 v1, vcc, 0, v1, vcc
	global_load_dword v1, v[0:1], off sc1

.Lskip_tab10:
	s_cmp_lg_u32 s44, 3
	s_mov_b64 s[4:5], 0
	s_waitcnt lgkmcnt(0)
	s_barrier
	s_cbranch_scc1 .LBB0_1659
	s_load_dwordx2 s[4:5], s[12:13], 0x90
